# MoE gather copy: all 4 token rows (8 dwordx4 loads) + 8 dest indices issued up front, then 16 stores with counted vmcnt (was per-row load/wait/store chain)
# speedup vs baseline: 1.0056x; 1.0056x over previous
; __global__ void __launch_bounds__(NWAVES * 64, 2) mk_fwd(Args a) {
;     ...
; #pragma unroll
;               for (int q = 0; q < 8; ++q) { const int i = wave * 8 + q, tok = bx * 32 + (i >> 1), dest = li[32 + i];
;                   const u32x4* s = (const u32x4*)((const unsigned char*)x1b + (size_t)tok * DM * EB); u32x4* d = (u32x4*)((unsigned char*)XG + (size_t)dest * DM * EB);
; #pragma unroll
;                   for (int jj = 0; jj < 2 * EB; ++jj) d[lane + 64 * jj] = s[lane + 64 * jj]; }
;               __syncthreads(); }
.LBB0_2197:
	v_readlane_b32 s1, v247, 0
	s_lshl_b32 s3, s1, 3
	s_lshl_b32 s12, s2, 5
	s_lshl_b32 s0, s1, 2
	s_lshl_b32 s1, s1, 5
	s_add_i32 s0, s0, s12
	s_add_i32 s1, s1, 0
	v_mov_b32_e32 v1, s1
	s_ashr_i32 s1, s0, 31
	s_lshl_b64 s[0:1], s[0:1], 11
	s_add_u32 s0, s62, s0
	s_addc_u32 s1, s63, s1
	v_lshlrev_b32_e32 v12, 4, v194
	s_waitcnt lgkmcnt(0)
	s_barrier
	ds_read_b32 v232, v1 offset:128
	ds_read_b32 v233, v1 offset:132
	ds_read_b32 v234, v1 offset:136
	ds_read_b32 v235, v1 offset:140
	ds_read_b32 v236, v1 offset:144
	ds_read_b32 v237, v1 offset:148
	ds_read_b32 v238, v1 offset:152
	ds_read_b32 v239, v1 offset:156
	s_add_u32 s100, s0, 0x1000
	s_addc_u32 s101, s1, 0
	global_load_dwordx4 v[200:203], v12, s[0:1]
	global_load_dwordx4 v[204:207], v12, s[0:1] offset:1024
	global_load_dwordx4 v[208:211], v12, s[0:1] offset:2048
	global_load_dwordx4 v[212:215], v12, s[0:1] offset:3072
	global_load_dwordx4 v[216:219], v12, s[100:101]
	global_load_dwordx4 v[220:223], v12, s[100:101] offset:1024
	global_load_dwordx4 v[224:227], v12, s[100:101] offset:2048
	global_load_dwordx4 v[228:231], v12, s[100:101] offset:3072
	s_waitcnt lgkmcnt(0)
	v_mov_b32_e32 v240, v232
	v_ashrrev_i32_e32 v241, 31, v232
	v_lshlrev_b64 v[240:241], 11, v[240:241]
	v_lshl_add_u64 v[240:241], s[42:43], 0, v[240:241]
	s_nop 0
	v_readfirstlane_b32 s12, v240
	v_readfirstlane_b32 s13, v241
	s_waitcnt vmcnt(6)
	s_nop 4
	global_store_dwordx4 v12, v[200:203], s[12:13]
	global_store_dwordx4 v12, v[204:207], s[12:13] offset:1024
	v_mov_b32_e32 v240, v233
	v_ashrrev_i32_e32 v241, 31, v233
	v_lshlrev_b64 v[240:241], 11, v[240:241]
	v_lshl_add_u64 v[240:241], s[42:43], 0, v[240:241]
	s_nop 0
	v_readfirstlane_b32 s12, v240
	v_readfirstlane_b32 s13, v241
	s_nop 4
	global_store_dwordx4 v12, v[200:203], s[12:13]
	global_store_dwordx4 v12, v[204:207], s[12:13] offset:1024
	v_mov_b32_e32 v240, v234
	v_ashrrev_i32_e32 v241, 31, v234
	v_lshlrev_b64 v[240:241], 11, v[240:241]
	v_lshl_add_u64 v[240:241], s[42:43], 0, v[240:241]
	s_nop 0
	v_readfirstlane_b32 s12, v240
	v_readfirstlane_b32 s13, v241
	s_waitcnt vmcnt(8)
	s_nop 4
	global_store_dwordx4 v12, v[208:211], s[12:13]
	global_store_dwordx4 v12, v[212:215], s[12:13] offset:1024
	v_mov_b32_e32 v240, v235
	v_ashrrev_i32_e32 v241, 31, v235
	v_lshlrev_b64 v[240:241], 11, v[240:241]
	v_lshl_add_u64 v[240:241], s[42:43], 0, v[240:241]
	s_nop 0
	v_readfirstlane_b32 s12, v240
	v_readfirstlane_b32 s13, v241
	s_nop 4
	global_store_dwordx4 v12, v[208:211], s[12:13]
	global_store_dwordx4 v12, v[212:215], s[12:13] offset:1024
	v_mov_b32_e32 v240, v236
	v_ashrrev_i32_e32 v241, 31, v236
	v_lshlrev_b64 v[240:241], 11, v[240:241]
	v_lshl_add_u64 v[240:241], s[42:43], 0, v[240:241]
	s_nop 0
	v_readfirstlane_b32 s12, v240
	v_readfirstlane_b32 s13, v241
	s_waitcnt vmcnt(10)
	s_nop 4
	global_store_dwordx4 v12, v[216:219], s[12:13]
	global_store_dwordx4 v12, v[220:223], s[12:13] offset:1024
	v_mov_b32_e32 v240, v237
	v_ashrrev_i32_e32 v241, 31, v237
	v_lshlrev_b64 v[240:241], 11, v[240:241]
	v_lshl_add_u64 v[240:241], s[42:43], 0, v[240:241]
	s_nop 0
	v_readfirstlane_b32 s12, v240
	v_readfirstlane_b32 s13, v241
	s_nop 4
	global_store_dwordx4 v12, v[216:219], s[12:13]
	global_store_dwordx4 v12, v[220:223], s[12:13] offset:1024
	v_mov_b32_e32 v240, v238
	v_ashrrev_i32_e32 v241, 31, v238
	v_lshlrev_b64 v[240:241], 11, v[240:241]
	v_lshl_add_u64 v[240:241], s[42:43], 0, v[240:241]
	s_nop 0
	v_readfirstlane_b32 s12, v240
	v_readfirstlane_b32 s13, v241
	s_waitcnt vmcnt(12)
	s_nop 4
	global_store_dwordx4 v12, v[224:227], s[12:13]
	global_store_dwordx4 v12, v[228:231], s[12:13] offset:1024
	v_mov_b32_e32 v240, v239
	v_ashrrev_i32_e32 v241, 31, v239
	v_lshlrev_b64 v[240:241], 11, v[240:241]
	v_lshl_add_u64 v[240:241], s[42:43], 0, v[240:241]
	s_nop 0
	v_readfirstlane_b32 s12, v240
	v_readfirstlane_b32 s13, v241
	s_nop 4
	global_store_dwordx4 v12, v[224:227], s[12:13]
	global_store_dwordx4 v12, v[228:231], s[12:13] offset:1024
	s_barrier
